# v50 + code placement: the five fp8 GEMM K-loop trip tops and their steady-state branch targets aligned to 64 bytes (padding sits behind unconditional branches, never executed)
# baseline (speedup 1.0000x reference)
.LBB0_981:
	s_add_i32 s89, s89, 1
	s_and_b32 s10, s89, 1
	s_lshl_b32 s10, s10, 2
	s_add_i32 s95, s10, 0
	s_mov_b32 s94, s36
	s_mov_b32 s93, s53
	s_mov_b32 s92, s54
	s_add_i32 s95, s95, 0x23f08
	s_mov_b64 s[34:35], 0
	s_mov_b32 s96, -2
	s_movk_i32 s97, 0x180
	v_mov_b32_e32 v0, 0
	v_mov_b32_e32 v1, v133
	v_mov_b32_e32 v2, v133
	v_mov_b32_e32 v3, v133
	v_mov_b32_e32 v4, 0
	v_mov_b32_e32 v5, v133
	v_mov_b32_e32 v6, v133
	v_mov_b32_e32 v7, v133
	v_mov_b32_e32 v12, 0
	v_mov_b32_e32 v13, v133
	v_mov_b32_e32 v14, v133
	v_mov_b32_e32 v15, v133
	v_mov_b32_e32 v20, 0
	v_mov_b32_e32 v21, v133
	v_mov_b32_e32 v22, v133
	v_mov_b32_e32 v23, v133
	v_mov_b32_e32 v28, 0
	v_mov_b32_e32 v29, v133
	v_mov_b32_e32 v30, v133
	v_mov_b32_e32 v31, v133
	v_mov_b32_e32 v36, 0
	v_mov_b32_e32 v37, v133
	v_mov_b32_e32 v38, v133
	v_mov_b32_e32 v39, v133
	v_mov_b32_e32 v44, 0
	v_mov_b32_e32 v45, v133
	v_mov_b32_e32 v46, v133
	v_mov_b32_e32 v47, v133
	v_mov_b32_e32 v52, 0
	v_mov_b32_e32 v53, v133
	v_mov_b32_e32 v54, v133
	v_mov_b32_e32 v55, v133
	v_mov_b32_e32 v8, 0
	v_mov_b32_e32 v9, v133
	v_mov_b32_e32 v10, v133
	v_mov_b32_e32 v11, v133
	v_mov_b32_e32 v16, 0
	v_mov_b32_e32 v17, v133
	v_mov_b32_e32 v18, v133
	v_mov_b32_e32 v19, v133
	v_mov_b32_e32 v24, 0
	v_mov_b32_e32 v25, v133
	v_mov_b32_e32 v26, v133
	v_mov_b32_e32 v27, v133
	v_mov_b32_e32 v32, 0
	v_mov_b32_e32 v33, v133
	v_mov_b32_e32 v34, v133
	v_mov_b32_e32 v35, v133
	v_mov_b32_e32 v40, 0
	v_mov_b32_e32 v41, v133
	v_mov_b32_e32 v42, v133
	v_mov_b32_e32 v43, v133
	v_mov_b32_e32 v48, 0
	v_mov_b32_e32 v49, v133
	v_mov_b32_e32 v50, v133
	v_mov_b32_e32 v51, v133
	v_mov_b32_e32 v56, 0
	v_mov_b32_e32 v57, v133
	v_mov_b32_e32 v58, v133
	v_mov_b32_e32 v59, v133
	v_mov_b32_e32 v60, 0
	v_mov_b32_e32 v61, v133
	v_mov_b32_e32 v62, v133
	v_mov_b32_e32 v63, v133
	v_mov_b32_e32 v64, 0
	v_mov_b32_e32 v65, v133
	v_mov_b32_e32 v66, v133
	v_mov_b32_e32 v67, v133
	v_mov_b32_e32 v68, 0
	v_mov_b32_e32 v69, v133
	v_mov_b32_e32 v70, v133
	v_mov_b32_e32 v71, v133
	v_mov_b32_e32 v76, 0
	v_mov_b32_e32 v77, v133
	v_mov_b32_e32 v78, v133
	v_mov_b32_e32 v79, v133
	v_mov_b32_e32 v84, 0
	v_mov_b32_e32 v85, v133
	v_mov_b32_e32 v86, v133
	v_mov_b32_e32 v87, v133
	v_mov_b32_e32 v92, 0
	v_mov_b32_e32 v93, v133
	v_mov_b32_e32 v94, v133
	v_mov_b32_e32 v95, v133
	v_mov_b32_e32 v100, 0
	v_mov_b32_e32 v101, v133
	v_mov_b32_e32 v102, v133
	v_mov_b32_e32 v103, v133
	v_mov_b32_e32 v108, 0
	v_mov_b32_e32 v109, v133
	v_mov_b32_e32 v110, v133
	v_mov_b32_e32 v111, v133
	v_mov_b32_e32 v116, 0
	v_mov_b32_e32 v117, v133
	v_mov_b32_e32 v118, v133
	v_mov_b32_e32 v119, v133
	v_mov_b32_e32 v72, 0
	v_mov_b32_e32 v73, v133
	v_mov_b32_e32 v74, v133
	v_mov_b32_e32 v75, v133
	v_mov_b32_e32 v80, 0
	v_mov_b32_e32 v81, v133
	v_mov_b32_e32 v82, v133
	v_mov_b32_e32 v83, v133
	v_mov_b32_e32 v88, 0
	v_mov_b32_e32 v89, v133
	v_mov_b32_e32 v90, v133
	v_mov_b32_e32 v91, v133
	v_mov_b32_e32 v96, 0
	v_mov_b32_e32 v97, v133
	v_mov_b32_e32 v98, v133
	v_mov_b32_e32 v99, v133
	v_mov_b32_e32 v104, 0
	v_mov_b32_e32 v105, v133
	v_mov_b32_e32 v106, v133
	v_mov_b32_e32 v107, v133
	v_mov_b32_e32 v112, 0
	v_mov_b32_e32 v113, v133
	v_mov_b32_e32 v114, v133
	v_mov_b32_e32 v115, v133
	v_mov_b32_e32 v120, 0
	v_mov_b32_e32 v121, v133
	v_mov_b32_e32 v122, v133
	v_mov_b32_e32 v123, v133
	v_mov_b32_e32 v124, 0
	v_mov_b32_e32 v125, v133
	v_mov_b32_e32 v126, v133
	v_mov_b32_e32 v127, v133
	s_branch .LBB0_983
	.p2align	6
.LBB0_982:
	s_cmpk_lg_i32 s97, 0x180
	s_cbranch_scc1 .Lp1_fast
	v_add_u32_e32 v129, s31, v128
	v_ashrrev_i32_e32 v131, 3, v129
	v_lshlrev_b32_e32 v130, 4, v128
	v_lshlrev_b32_e32 v136, 1, v131
	v_lshrrev_b32_e32 v137, 2, v131
	v_bitop3_b32 v130, v129, s55, v130 bitop3:0x48
	v_and_b32_e32 v136, 24, v136
	v_and_b32_e32 v137, 4, v137
	v_and_b32_e32 v138, 0x1fffe3, v131
	v_lshl_add_u32 v129, v129, 4, v132
	v_or3_b32 v136, v138, v137, v136
	v_ashrrev_i32_e32 v129, 7, v129
	v_lshl_or_b32 v244, v136, 11, v130
	v_lshlrev_b32_e32 v136, 1, v129
	v_lshrrev_b32_e32 v137, 2, v129
	v_and_b32_e32 v136, 24, v136
	v_and_b32_e32 v137, 4, v137
	v_and_b32_e32 v138, 0x1fffe3, v129
	v_or3_b32 v136, v138, v137, v136
	v_lshl_or_b32 v245, v136, 11, v130
	v_and_b32_e32 v136, 15, v128
	v_lshrrev_b32_e32 v137, 3, v128
	v_bfe_u32 v128, v128, 1, 3
	s_mov_b32 s10, 0xffffffe
	v_lshlrev_b32_e32 v136, 7, v136
	v_and_b32_e32 v138, 0xffffffe, v137
	v_bitop3_b32 v137, v137, v128, s10 bitop3:0x6c
	v_or_b32_e32 v168, s70, v136
	v_or_b32_e32 v136, s71, v136
	v_lshlrev_b32_e32 v169, 4, v137
	v_bitop3_b32 v128, v138, v128, 1 bitop3:0x36
	v_add_u32_e32 v246, v169, v136
	v_lshlrev_b32_e32 v128, 4, v128
	v_add_u32_e32 v247, v128, v136
	v_lshl_or_b32 v249, v129, 11, v130
	v_add_u32_e32 v129, s85, v246
	v_lshl_or_b32 v248, v131, 11, v130
	v_add_u32_e32 v130, s85, v247
	v_add_u32_e32 v250, 0x40000, v248
	v_add_u32_e32 v251, 0x40000, v249
	v_add3_u32 v252, v169, v168, 0
	v_add3_u32 v253, v128, v168, 0
	s_branch .Lp1_join
	.p2align	6

.LBB0_2172:
	s_add_i32 s53, s53, 1
	s_mul_i32 s6, s53, s86
	s_add_i32 s6, s6, s96
	s_cmpk_lt_i32 s6, 0x200
	s_cselect_b64 s[20:21], -1, 0
	s_ashr_i32 s7, s6, 31
	s_lshr_b32 s7, s7, 29
	s_add_i32 s7, s6, s7
	s_ashr_i32 s18, s7, 3
	s_and_b32 s7, s7, -8
	s_sub_i32 s6, s6, s7
	s_lshl_b32 s7, s6, 6
	s_cmp_lt_i32 s6, 0
	s_mulk_i32 s6, 0x41
	s_cselect_b32 s6, s6, s7
	s_add_i32 s6, s6, s18
	s_ashr_i32 s7, s6, 31
	s_lshr_b32 s7, s7, 26
	s_add_i32 s7, s6, s7
	s_ashr_i32 s18, s7, 6
	s_and_b32 s7, s7, 0xffc0
	s_sub_i32 s6, s6, s7
	s_bfe_i32 s7, s6, 0x80000
	s_bfe_u32 s7, s7, 0x3000c
	s_add_i32 s7, s6, s7
	s_lshl_b32 s58, s18, 3
	s_bfe_i32 s18, s7, 0x80000
	s_and_b32 s7, s7, 0xf8
	s_sext_i32_i16 s18, s18
	s_sub_i32 s6, s6, s7
	s_sext_i32_i8 s6, s6
	s_ashr_i32 s59, s18, 3
	v_mov_b32_e32 v0, 0
	s_mov_b32 s57, s29
	s_mov_b32 s56, s23
	s_mov_b32 s55, s24
	s_add_i32 s58, s58, s6
	s_lshl_b32 s60, s59, 19
	s_mov_b64 s[18:19], 0
	s_mov_b32 s61, -2
	s_movk_i32 s62, 0x180
	v_mov_b32_e32 v1, v0
	v_mov_b32_e32 v2, v0
	v_mov_b32_e32 v3, v0
	v_mov_b32_e32 v4, v0
	v_mov_b32_e32 v5, v0
	v_mov_b32_e32 v6, v0
	v_mov_b32_e32 v7, v0
	v_mov_b32_e32 v16, v0
	v_mov_b32_e32 v17, v0
	v_mov_b32_e32 v18, v0
	v_mov_b32_e32 v19, v0
	v_mov_b32_e32 v20, v0
	v_mov_b32_e32 v21, v0
	v_mov_b32_e32 v22, v0
	v_mov_b32_e32 v23, v0
	v_mov_b32_e32 v32, v0
	v_mov_b32_e32 v33, v0
	v_mov_b32_e32 v34, v0
	v_mov_b32_e32 v35, v0
	v_mov_b32_e32 v36, v0
	v_mov_b32_e32 v37, v0
	v_mov_b32_e32 v38, v0
	v_mov_b32_e32 v39, v0
	v_mov_b32_e32 v48, v0
	v_mov_b32_e32 v49, v0
	v_mov_b32_e32 v50, v0
	v_mov_b32_e32 v51, v0
	v_mov_b32_e32 v52, v0
	v_mov_b32_e32 v53, v0
	v_mov_b32_e32 v54, v0
	v_mov_b32_e32 v55, v0
	v_mov_b32_e32 v8, v0
	v_mov_b32_e32 v9, v0
	v_mov_b32_e32 v10, v0
	v_mov_b32_e32 v11, v0
	v_mov_b32_e32 v12, v0
	v_mov_b32_e32 v13, v0
	v_mov_b32_e32 v14, v0
	v_mov_b32_e32 v15, v0
	v_mov_b32_e32 v24, v0
	v_mov_b32_e32 v25, v0
	v_mov_b32_e32 v26, v0
	v_mov_b32_e32 v27, v0
	v_mov_b32_e32 v28, v0
	v_mov_b32_e32 v29, v0
	v_mov_b32_e32 v30, v0
	v_mov_b32_e32 v31, v0
	v_mov_b32_e32 v40, v0
	v_mov_b32_e32 v41, v0
	v_mov_b32_e32 v42, v0
	v_mov_b32_e32 v43, v0
	v_mov_b32_e32 v44, v0
	v_mov_b32_e32 v45, v0
	v_mov_b32_e32 v46, v0
	v_mov_b32_e32 v47, v0
	v_mov_b32_e32 v56, v0
	v_mov_b32_e32 v57, v0
	v_mov_b32_e32 v58, v0
	v_mov_b32_e32 v59, v0
	v_mov_b32_e32 v60, v0
	v_mov_b32_e32 v61, v0
	v_mov_b32_e32 v62, v0
	v_mov_b32_e32 v63, v0
	v_mov_b32_e32 v64, v0
	v_mov_b32_e32 v65, v0
	v_mov_b32_e32 v66, v0
	v_mov_b32_e32 v67, v0
	v_mov_b32_e32 v68, v0
	v_mov_b32_e32 v69, v0
	v_mov_b32_e32 v70, v0
	v_mov_b32_e32 v71, v0
	v_mov_b32_e32 v80, v0
	v_mov_b32_e32 v81, v0
	v_mov_b32_e32 v82, v0
	v_mov_b32_e32 v83, v0
	v_mov_b32_e32 v84, v0
	v_mov_b32_e32 v85, v0
	v_mov_b32_e32 v86, v0
	v_mov_b32_e32 v87, v0
	v_mov_b32_e32 v96, v0
	v_mov_b32_e32 v97, v0
	v_mov_b32_e32 v98, v0
	v_mov_b32_e32 v99, v0
	v_mov_b32_e32 v100, v0
	v_mov_b32_e32 v101, v0
	v_mov_b32_e32 v102, v0
	v_mov_b32_e32 v103, v0
	v_mov_b32_e32 v112, v0
	v_mov_b32_e32 v113, v0
	v_mov_b32_e32 v114, v0
	v_mov_b32_e32 v115, v0
	v_mov_b32_e32 v116, v0
	v_mov_b32_e32 v117, v0
	v_mov_b32_e32 v118, v0
	v_mov_b32_e32 v119, v0
	v_mov_b32_e32 v72, v0
	v_mov_b32_e32 v73, v0
	v_mov_b32_e32 v74, v0
	v_mov_b32_e32 v75, v0
	v_mov_b32_e32 v76, v0
	v_mov_b32_e32 v77, v0
	v_mov_b32_e32 v78, v0
	v_mov_b32_e32 v79, v0
	v_mov_b32_e32 v88, v0
	v_mov_b32_e32 v89, v0
	v_mov_b32_e32 v90, v0
	v_mov_b32_e32 v91, v0
	v_mov_b32_e32 v92, v0
	v_mov_b32_e32 v93, v0
	v_mov_b32_e32 v94, v0
	v_mov_b32_e32 v95, v0
	v_mov_b32_e32 v104, v0
	v_mov_b32_e32 v105, v0
	v_mov_b32_e32 v106, v0
	v_mov_b32_e32 v107, v0
	v_mov_b32_e32 v108, v0
	v_mov_b32_e32 v109, v0
	v_mov_b32_e32 v110, v0
	v_mov_b32_e32 v111, v0
	v_mov_b32_e32 v120, v0
	v_mov_b32_e32 v121, v0
	v_mov_b32_e32 v122, v0
	v_mov_b32_e32 v123, v0
	v_mov_b32_e32 v124, v0
	v_mov_b32_e32 v125, v0
	v_mov_b32_e32 v126, v0
	v_mov_b32_e32 v127, v0
	s_branch .LBB0_2174
	.p2align	6
.LBB0_2173:
	s_cmpk_lg_i32 s62, 0x180
	s_cbranch_scc1 .Lp5_fast
	v_add_u32_e32 v129, s17, v128
	v_lshlrev_b32_e32 v130, 4, v128
	v_ashrrev_i32_e32 v131, 3, v129
	v_bitop3_b32 v130, v129, s22, v130 bitop3:0x48
	v_lshlrev_b32_e32 v132, 1, v131
	v_lshrrev_b32_e32 v133, 2, v131
	v_lshl_add_u32 v129, v129, 4, v134
	v_and_b32_e32 v132, 24, v132
	v_and_b32_e32 v133, 4, v133
	v_and_b32_e32 v136, 0x1fffe3, v131
	v_ashrrev_i32_e32 v129, 7, v129
	v_or3_b32 v132, v136, v133, v132
	v_lshlrev_b32_e32 v133, 1, v129
	v_lshrrev_b32_e32 v136, 2, v129
	v_and_b32_e32 v133, 24, v133
	v_and_b32_e32 v136, 4, v136
	v_and_b32_e32 v137, 0x1fffe3, v129
	v_or3_b32 v133, v137, v136, v133
	v_and_b32_e32 v136, 15, v128
	v_lshrrev_b32_e32 v137, 3, v128
	v_bfe_u32 v128, v128, 1, 3
	v_lshlrev_b32_e32 v136, 7, v136
	v_and_b32_e32 v138, 0xffffffe, v137
	v_bitop3_b32 v137, v137, v128, s48 bitop3:0x6c
	v_or_b32_e32 v168, s42, v136
	v_or_b32_e32 v136, s43, v136
	v_lshlrev_b32_e32 v169, 4, v137
	v_bitop3_b32 v128, v138, v128, 1 bitop3:0x36
	v_add_u32_e32 v244, v169, v136
	v_lshlrev_b32_e32 v128, 4, v128
	v_add_u32_e32 v245, v128, v136
	v_lshl_or_b32 v247, v129, 11, v130
	v_add_u32_e32 v129, s49, v244
	v_lshl_or_b32 v132, v132, 11, v130
	v_lshl_or_b32 v133, v133, 11, v130
	v_lshl_or_b32 v246, v131, 11, v130
	v_add_u32_e32 v130, s49, v245
	v_add_u32_e32 v248, 0x40000, v246
	v_add_u32_e32 v249, 0x40000, v247
	v_add3_u32 v250, v169, v168, 0
	v_add3_u32 v251, v128, v168, 0
	s_branch .Lp5_join
	.p2align	6

.LBB0_2196:
	s_add_i32 s55, s55, 1
	s_mul_i32 s6, s55, s86
	s_add_i32 s6, s6, s96
	s_cmpk_lt_i32 s6, 0x200
	s_cselect_b64 s[22:23], -1, 0
	s_ashr_i32 s7, s6, 31
	s_lshr_b32 s7, s7, 29
	s_add_i32 s7, s6, s7
	s_ashr_i32 s20, s7, 3
	s_and_b32 s7, s7, -8
	s_sub_i32 s6, s6, s7
	s_lshl_b32 s7, s6, 6
	s_cmp_lt_i32 s6, 0
	s_mulk_i32 s6, 0x41
	s_cselect_b32 s6, s6, s7
	s_add_i32 s6, s6, s20
	s_ashr_i32 s7, s6, 31
	s_lshr_b32 s7, s7, 26
	s_add_i32 s7, s6, s7
	s_ashr_i32 s20, s7, 6
	s_and_b32 s7, s7, 0xffc0
	s_sub_i32 s6, s6, s7
	s_bfe_i32 s7, s6, 0x80000
	s_bfe_u32 s7, s7, 0x3000c
	s_add_i32 s7, s6, s7
	s_lshl_b32 s60, s20, 3
	s_bfe_i32 s20, s7, 0x80000
	s_and_b32 s7, s7, 0xf8
	s_sext_i32_i16 s20, s20
	s_sub_i32 s6, s6, s7
	s_sext_i32_i8 s6, s6
	s_ashr_i32 s61, s20, 3
	s_mov_b32 s59, s31
	s_mov_b32 s58, s25
	s_mov_b32 s57, s26
	s_add_i32 s60, s60, s6
	s_lshl_b32 s62, s61, 19
	s_mov_b64 s[20:21], 0
	s_mov_b32 s63, -2
	s_movk_i32 s64, 0x180
	v_mov_b32_e32 v0, 0
	v_mov_b32_e32 v1, v158
	v_mov_b32_e32 v2, v158
	v_mov_b32_e32 v3, v158
	v_mov_b32_e32 v4, 0
	v_mov_b32_e32 v5, v158
	v_mov_b32_e32 v6, v158
	v_mov_b32_e32 v7, v158
	v_mov_b32_e32 v16, 0
	v_mov_b32_e32 v17, v158
	v_mov_b32_e32 v18, v158
	v_mov_b32_e32 v19, v158
	v_mov_b32_e32 v20, 0
	v_mov_b32_e32 v21, v158
	v_mov_b32_e32 v22, v158
	v_mov_b32_e32 v23, v158
	v_mov_b32_e32 v32, 0
	v_mov_b32_e32 v33, v158
	v_mov_b32_e32 v34, v158
	v_mov_b32_e32 v35, v158
	v_mov_b32_e32 v36, 0
	v_mov_b32_e32 v37, v158
	v_mov_b32_e32 v38, v158
	v_mov_b32_e32 v39, v158
	v_mov_b32_e32 v48, 0
	v_mov_b32_e32 v49, v158
	v_mov_b32_e32 v50, v158
	v_mov_b32_e32 v51, v158
	v_mov_b32_e32 v52, 0
	v_mov_b32_e32 v53, v158
	v_mov_b32_e32 v54, v158
	v_mov_b32_e32 v55, v158
	v_mov_b32_e32 v8, 0
	v_mov_b32_e32 v9, v158
	v_mov_b32_e32 v10, v158
	v_mov_b32_e32 v11, v158
	v_mov_b32_e32 v12, 0
	v_mov_b32_e32 v13, v158
	v_mov_b32_e32 v14, v158
	v_mov_b32_e32 v15, v158
	v_mov_b32_e32 v24, 0
	v_mov_b32_e32 v25, v158
	v_mov_b32_e32 v26, v158
	v_mov_b32_e32 v27, v158
	v_mov_b32_e32 v28, 0
	v_mov_b32_e32 v29, v158
	v_mov_b32_e32 v30, v158
	v_mov_b32_e32 v31, v158
	v_mov_b32_e32 v40, 0
	v_mov_b32_e32 v41, v158
	v_mov_b32_e32 v42, v158
	v_mov_b32_e32 v43, v158
	v_mov_b32_e32 v44, 0
	v_mov_b32_e32 v45, v158
	v_mov_b32_e32 v46, v158
	v_mov_b32_e32 v47, v158
	v_mov_b32_e32 v56, 0
	v_mov_b32_e32 v57, v158
	v_mov_b32_e32 v58, v158
	v_mov_b32_e32 v59, v158
	v_mov_b32_e32 v60, 0
	v_mov_b32_e32 v61, v158
	v_mov_b32_e32 v62, v158
	v_mov_b32_e32 v63, v158
	v_mov_b32_e32 v64, 0
	v_mov_b32_e32 v65, v158
	v_mov_b32_e32 v66, v158
	v_mov_b32_e32 v67, v158
	v_mov_b32_e32 v68, 0
	v_mov_b32_e32 v69, v158
	v_mov_b32_e32 v70, v158
	v_mov_b32_e32 v71, v158
	v_mov_b32_e32 v80, 0
	v_mov_b32_e32 v81, v158
	v_mov_b32_e32 v82, v158
	v_mov_b32_e32 v83, v158
	v_mov_b32_e32 v84, 0
	v_mov_b32_e32 v85, v158
	v_mov_b32_e32 v86, v158
	v_mov_b32_e32 v87, v158
	v_mov_b32_e32 v96, 0
	v_mov_b32_e32 v97, v158
	v_mov_b32_e32 v98, v158
	v_mov_b32_e32 v99, v158
	v_mov_b32_e32 v100, 0
	v_mov_b32_e32 v101, v158
	v_mov_b32_e32 v102, v158
	v_mov_b32_e32 v103, v158
	v_mov_b32_e32 v112, 0
	v_mov_b32_e32 v113, v158
	v_mov_b32_e32 v114, v158
	v_mov_b32_e32 v115, v158
	v_mov_b32_e32 v116, 0
	v_mov_b32_e32 v117, v158
	v_mov_b32_e32 v118, v158
	v_mov_b32_e32 v119, v158
	v_mov_b32_e32 v72, 0
	v_mov_b32_e32 v73, v158
	v_mov_b32_e32 v74, v158
	v_mov_b32_e32 v75, v158
	v_mov_b32_e32 v76, 0
	v_mov_b32_e32 v77, v158
	v_mov_b32_e32 v78, v158
	v_mov_b32_e32 v79, v158
	v_mov_b32_e32 v88, 0
	v_mov_b32_e32 v89, v158
	v_mov_b32_e32 v90, v158
	v_mov_b32_e32 v91, v158
	v_mov_b32_e32 v92, 0
	v_mov_b32_e32 v93, v158
	v_mov_b32_e32 v94, v158
	v_mov_b32_e32 v95, v158
	v_mov_b32_e32 v104, 0
	v_mov_b32_e32 v105, v158
	v_mov_b32_e32 v106, v158
	v_mov_b32_e32 v107, v158
	v_mov_b32_e32 v108, 0
	v_mov_b32_e32 v109, v158
	v_mov_b32_e32 v110, v158
	v_mov_b32_e32 v111, v158
	v_mov_b32_e32 v120, 0
	v_mov_b32_e32 v121, v158
	v_mov_b32_e32 v122, v158
	v_mov_b32_e32 v123, v158
	v_mov_b32_e32 v124, 0
	v_mov_b32_e32 v125, v158
	v_mov_b32_e32 v126, v158
	v_mov_b32_e32 v127, v158
	s_branch .LBB0_2198
	.p2align	6
.LBB0_2197:
	s_cmpk_lg_i32 s64, 0x180
	s_cbranch_scc1 .Lp6_fast
	v_add_u32_e32 v129, s19, v128
	v_ashrrev_i32_e32 v131, 3, v129
	v_lshlrev_b32_e32 v130, 4, v128
	v_lshlrev_b32_e32 v132, 1, v131
	v_lshrrev_b32_e32 v133, 2, v131
	v_bitop3_b32 v130, v129, s24, v130 bitop3:0x48
	v_and_b32_e32 v132, 24, v132
	v_and_b32_e32 v133, 4, v133
	v_and_b32_e32 v134, 0x1fffe3, v131
	v_lshl_add_u32 v129, v129, 4, v156
	v_or3_b32 v132, v134, v133, v132
	v_ashrrev_i32_e32 v129, 7, v129
	v_lshl_or_b32 v159, v132, 11, v130
	v_lshlrev_b32_e32 v132, 1, v129
	v_lshrrev_b32_e32 v133, 2, v129
	v_and_b32_e32 v132, 24, v132
	v_and_b32_e32 v133, 4, v133
	v_and_b32_e32 v134, 0x1fffe3, v129
	v_or3_b32 v132, v134, v133, v132
	v_lshrrev_b32_e32 v133, 3, v128
	v_lshl_or_b32 v244, v132, 11, v130
	v_and_b32_e32 v132, 15, v128
	v_and_b32_e32 v134, 0xffffffe, v133
	v_bfe_u32 v128, v128, 1, 3
	v_lshlrev_b32_e32 v132, 7, v132
	v_bitop3_b32 v133, v133, v128, s50 bitop3:0x6c
	v_bitop3_b32 v128, v134, v128, 1 bitop3:0x36
	v_or_b32_e32 v152, s44, v132
	v_or_b32_e32 v132, s45, v132
	v_lshlrev_b32_e32 v153, 4, v133
	v_lshlrev_b32_e32 v154, 4, v128
	v_add_u32_e32 v245, v153, v132
	v_add_u32_e32 v246, v154, v132
	v_add_u32_e32 v132, s51, v245
	v_add_u32_e32 v140, s51, v246
	v_add_u32_e32 v148, s52, v245
	v_lshl_or_b32 v247, v131, 11, v130
	v_lshl_or_b32 v248, v129, 11, v130
	v_add_u32_e32 v249, 0x40000, v247
	v_add_u32_e32 v250, 0x40000, v248
	v_add3_u32 v251, v153, v152, 0
	v_add3_u32 v252, v154, v152, 0
	s_branch .Lp6_join
	.p2align	6

.LBB0_2274:
	s_add_i32 s52, s52, 1
	s_mul_i32 s6, s52, s86
	s_add_i32 s6, s6, s96
	s_cmpk_lt_i32 s6, 0x200
	s_cselect_b64 s[20:21], -1, 0
	s_ashr_i32 s7, s6, 31
	s_lshr_b32 s7, s7, 29
	s_add_i32 s7, s6, s7
	s_ashr_i32 s18, s7, 3
	s_and_b32 s7, s7, -8
	s_sub_i32 s6, s6, s7
	s_lshl_b32 s7, s6, 6
	s_cmp_lt_i32 s6, 0
	s_mulk_i32 s6, 0x41
	s_cselect_b32 s6, s6, s7
	s_add_i32 s6, s6, s18
	s_ashr_i32 s7, s6, 31
	s_lshr_b32 s7, s7, 26
	s_add_i32 s7, s6, s7
	s_ashr_i32 s18, s7, 6
	s_and_b32 s7, s7, 0xffc0
	s_sub_i32 s6, s6, s7
	s_bfe_i32 s7, s6, 0x80000
	s_bfe_u32 s7, s7, 0x3000c
	s_add_i32 s7, s6, s7
	s_lshl_b32 s57, s18, 3
	s_bfe_i32 s18, s7, 0x80000
	s_and_b32 s7, s7, 0xf8
	s_sext_i32_i16 s18, s18
	s_sub_i32 s6, s6, s7
	s_sext_i32_i8 s6, s6
	s_ashr_i32 s58, s18, 3
	v_mov_b32_e32 v0, 0
	s_mov_b32 s56, s29
	s_mov_b32 s55, s23
	s_mov_b32 s54, s24
	s_add_i32 s57, s57, s6
	s_lshl_b32 s59, s58, 19
	s_mov_b64 s[18:19], 0
	s_mov_b32 s60, -2
	s_movk_i32 s61, 0x180
	v_mov_b32_e32 v1, v0
	v_mov_b32_e32 v2, v0
	v_mov_b32_e32 v3, v0
	v_mov_b32_e32 v4, v0
	v_mov_b32_e32 v5, v0
	v_mov_b32_e32 v6, v0
	v_mov_b32_e32 v7, v0
	v_mov_b32_e32 v8, v0
	v_mov_b32_e32 v9, v0
	v_mov_b32_e32 v10, v0
	v_mov_b32_e32 v11, v0
	v_mov_b32_e32 v12, v0
	v_mov_b32_e32 v13, v0
	v_mov_b32_e32 v14, v0
	v_mov_b32_e32 v15, v0
	v_mov_b32_e32 v32, v0
	v_mov_b32_e32 v33, v0
	v_mov_b32_e32 v34, v0
	v_mov_b32_e32 v35, v0
	v_mov_b32_e32 v36, v0
	v_mov_b32_e32 v37, v0
	v_mov_b32_e32 v38, v0
	v_mov_b32_e32 v39, v0
	v_mov_b32_e32 v40, v0
	v_mov_b32_e32 v41, v0
	v_mov_b32_e32 v42, v0
	v_mov_b32_e32 v43, v0
	v_mov_b32_e32 v44, v0
	v_mov_b32_e32 v45, v0
	v_mov_b32_e32 v46, v0
	v_mov_b32_e32 v47, v0
	v_mov_b32_e32 v16, v0
	v_mov_b32_e32 v17, v0
	v_mov_b32_e32 v18, v0
	v_mov_b32_e32 v19, v0
	v_mov_b32_e32 v20, v0
	v_mov_b32_e32 v21, v0
	v_mov_b32_e32 v22, v0
	v_mov_b32_e32 v23, v0
	v_mov_b32_e32 v24, v0
	v_mov_b32_e32 v25, v0
	v_mov_b32_e32 v26, v0
	v_mov_b32_e32 v27, v0
	v_mov_b32_e32 v28, v0
	v_mov_b32_e32 v29, v0
	v_mov_b32_e32 v30, v0
	v_mov_b32_e32 v31, v0
	v_mov_b32_e32 v48, v0
	v_mov_b32_e32 v49, v0
	v_mov_b32_e32 v50, v0
	v_mov_b32_e32 v51, v0
	v_mov_b32_e32 v52, v0
	v_mov_b32_e32 v53, v0
	v_mov_b32_e32 v54, v0
	v_mov_b32_e32 v55, v0
	v_mov_b32_e32 v56, v0
	v_mov_b32_e32 v57, v0
	v_mov_b32_e32 v58, v0
	v_mov_b32_e32 v59, v0
	v_mov_b32_e32 v60, v0
	v_mov_b32_e32 v61, v0
	v_mov_b32_e32 v62, v0
	v_mov_b32_e32 v63, v0
	v_mov_b32_e32 v64, v0
	v_mov_b32_e32 v65, v0
	v_mov_b32_e32 v66, v0
	v_mov_b32_e32 v67, v0
	v_mov_b32_e32 v68, v0
	v_mov_b32_e32 v69, v0
	v_mov_b32_e32 v70, v0
	v_mov_b32_e32 v71, v0
	v_mov_b32_e32 v72, v0
	v_mov_b32_e32 v73, v0
	v_mov_b32_e32 v74, v0
	v_mov_b32_e32 v75, v0
	v_mov_b32_e32 v76, v0
	v_mov_b32_e32 v77, v0
	v_mov_b32_e32 v78, v0
	v_mov_b32_e32 v79, v0
	v_mov_b32_e32 v96, v0
	v_mov_b32_e32 v97, v0
	v_mov_b32_e32 v98, v0
	v_mov_b32_e32 v99, v0
	v_mov_b32_e32 v100, v0
	v_mov_b32_e32 v101, v0
	v_mov_b32_e32 v102, v0
	v_mov_b32_e32 v103, v0
	v_mov_b32_e32 v104, v0
	v_mov_b32_e32 v105, v0
	v_mov_b32_e32 v106, v0
	v_mov_b32_e32 v107, v0
	v_mov_b32_e32 v108, v0
	v_mov_b32_e32 v109, v0
	v_mov_b32_e32 v110, v0
	v_mov_b32_e32 v111, v0
	v_mov_b32_e32 v80, v0
	v_mov_b32_e32 v81, v0
	v_mov_b32_e32 v82, v0
	v_mov_b32_e32 v83, v0
	v_mov_b32_e32 v84, v0
	v_mov_b32_e32 v85, v0
	v_mov_b32_e32 v86, v0
	v_mov_b32_e32 v87, v0
	v_mov_b32_e32 v88, v0
	v_mov_b32_e32 v89, v0
	v_mov_b32_e32 v90, v0
	v_mov_b32_e32 v91, v0
	v_mov_b32_e32 v92, v0
	v_mov_b32_e32 v93, v0
	v_mov_b32_e32 v94, v0
	v_mov_b32_e32 v95, v0
	v_mov_b32_e32 v112, v0
	v_mov_b32_e32 v113, v0
	v_mov_b32_e32 v114, v0
	v_mov_b32_e32 v115, v0
	v_mov_b32_e32 v116, v0
	v_mov_b32_e32 v117, v0
	v_mov_b32_e32 v118, v0
	v_mov_b32_e32 v119, v0
	v_mov_b32_e32 v120, v0
	v_mov_b32_e32 v121, v0
	v_mov_b32_e32 v122, v0
	v_mov_b32_e32 v123, v0
	v_mov_b32_e32 v124, v0
	v_mov_b32_e32 v125, v0
	v_mov_b32_e32 v126, v0
	v_mov_b32_e32 v127, v0
	s_branch .LBB0_2276
	.p2align	6
.LBB0_2275:
	s_cmpk_lg_i32 s61, 0x180
	s_cbranch_scc1 .Lp7_fast
	v_add_u32_e32 v129, s17, v128
	v_ashrrev_i32_e32 v131, 3, v129
	v_lshlrev_b32_e32 v130, 4, v128
	v_lshlrev_b32_e32 v132, 1, v131
	v_lshrrev_b32_e32 v133, 2, v131
	v_bitop3_b32 v130, v129, s22, v130 bitop3:0x48
	v_and_b32_e32 v132, 24, v132
	v_and_b32_e32 v133, 4, v133
	v_and_b32_e32 v134, 0x1fffe3, v131
	v_lshl_add_u32 v129, v129, 4, v136
	v_or3_b32 v132, v134, v133, v132
	v_ashrrev_i32_e32 v129, 7, v129
	v_lshl_or_b32 v242, v132, 11, v130
	v_lshlrev_b32_e32 v132, 1, v129
	v_lshrrev_b32_e32 v133, 2, v129
	v_and_b32_e32 v132, 24, v132
	v_and_b32_e32 v133, 4, v133
	v_and_b32_e32 v134, 0x1fffe3, v129
	v_or3_b32 v132, v134, v133, v132
	v_lshrrev_b32_e32 v133, 3, v128
	v_lshl_or_b32 v243, v132, 11, v130
	v_and_b32_e32 v132, 15, v128
	v_and_b32_e32 v134, 0xffffffe, v133
	v_bfe_u32 v128, v128, 1, 3
	v_lshlrev_b32_e32 v132, 7, v132
	v_bitop3_b32 v133, v133, v128, s48 bitop3:0x6c
	v_bitop3_b32 v128, v134, v128, 1 bitop3:0x36
	v_or_b32_e32 v162, s42, v132
	v_or_b32_e32 v132, s43, v132
	v_lshlrev_b32_e32 v163, 4, v133
	v_lshlrev_b32_e32 v164, 4, v128
	v_add_u32_e32 v244, v163, v132
	v_add_u32_e32 v245, v164, v132
	v_add_u32_e32 v132, s49, v244
	v_add_u32_e32 v142, s49, v245
	v_add_u32_e32 v150, s50, v244
	v_add_u32_e32 v158, s50, v245
	v_lshl_or_b32 v246, v131, 11, v130
	v_lshl_or_b32 v247, v129, 11, v130
	v_add_u32_e32 v248, 0x40000, v246
	v_add_u32_e32 v249, 0x40000, v247
	v_add3_u32 v250, v163, v162, 0
	v_add3_u32 v251, v164, v162, 0
	s_branch .Lp7_join
	.p2align	6

.LBB0_2567:
	s_add_i32 s70, s70, 1
	s_mul_i32 s6, s70, s86
	s_add_i32 s6, s6, s96
	s_cmp_lt_i32 s6, s33
	s_cselect_b64 s[30:31], -1, 0
	s_ashr_i32 s7, s6, 31
	s_lshr_b32 s7, s7, 29
	s_add_i32 s7, s6, s7
	s_ashr_i32 s10, s7, 3
	s_and_b32 s7, s7, -8
	s_sub_i32 s6, s6, s7
	s_cmp_lt_i32 s6, 0
	s_cselect_b32 s7, s38, s19
	s_mul_i32 s6, s6, s7
	s_add_i32 s6, s6, s10
	s_ashr_i32 s7, s6, 31
	s_lshr_b32 s7, s7, 26
	s_add_i32 s7, s6, s7
	s_ashr_i32 s10, s7, 6
	s_lshl_b32 s11, s10, 3
	s_sub_i32 s11, s19, s11
	s_min_i32 s11, s11, 8
	s_abs_i32 s28, s11
	v_cvt_f32_u32_e32 v0, s28
	s_sub_i32 s76, 0, s28
	s_andn2_b32 s7, s7, 63
	s_sub_i32 s6, s6, s7
	v_rcp_iflag_f32_e32 v0, v0
	s_abs_i32 s29, s6
	s_lshl_b32 s7, s10, 5
	s_xor_b32 s10, s6, s11
	v_mul_f32_e32 v0, 0x4f7ffffe, v0
	v_cvt_u32_f32_e32 v0, v0
	s_add_i32 s7, s7, 0
	s_ashr_i32 s10, s10, 31
	s_mov_b32 s75, s51
	v_readfirstlane_b32 s77, v0
	s_mul_i32 s76, s76, s77
	s_mul_hi_u32 s76, s77, s76
	s_add_i32 s77, s77, s76
	s_mul_hi_u32 s76, s29, s77
	s_mul_i32 s77, s76, s28
	s_sub_i32 s29, s29, s77
	s_add_i32 s77, s76, 1
	s_sub_i32 s78, s29, s28
	s_cmp_ge_u32 s29, s28
	s_cselect_b32 s76, s77, s76
	s_cselect_b32 s29, s78, s29
	s_add_i32 s77, s76, 1
	s_cmp_ge_u32 s29, s28
	s_cselect_b32 s28, s77, s76
	s_xor_b32 s28, s28, s10
	s_sub_i32 s76, s28, s10
	s_mul_i32 s10, s76, s11
	s_sub_i32 s6, s6, s10
	s_lshl_b32 s6, s6, 2
	s_add_i32 s77, s7, s6
	s_mov_b32 s74, s40
	s_mov_b32 s73, s39
	s_mov_b32 s34, s41
	s_add_i32 s77, s77, 0x22000
	s_lshl_b32 s78, s76, 19
	s_mov_b64 s[28:29], 0
	s_mov_b32 s79, -2
	s_movk_i32 s80, 0x180
	v_mov_b32_e32 v0, 0
	v_mov_b32_e32 v1, v153
	v_mov_b32_e32 v2, v153
	v_mov_b32_e32 v3, v153
	v_mov_b32_e32 v4, 0
	v_mov_b32_e32 v5, v153
	v_mov_b32_e32 v6, v153
	v_mov_b32_e32 v7, v153
	v_mov_b32_e32 v12, 0
	v_mov_b32_e32 v13, v153
	v_mov_b32_e32 v14, v153
	v_mov_b32_e32 v15, v153
	v_mov_b32_e32 v20, 0
	v_mov_b32_e32 v21, v153
	v_mov_b32_e32 v22, v153
	v_mov_b32_e32 v23, v153
	v_mov_b32_e32 v28, 0
	v_mov_b32_e32 v29, v153
	v_mov_b32_e32 v30, v153
	v_mov_b32_e32 v31, v153
	v_mov_b32_e32 v36, 0
	v_mov_b32_e32 v37, v153
	v_mov_b32_e32 v38, v153
	v_mov_b32_e32 v39, v153
	v_mov_b32_e32 v44, 0
	v_mov_b32_e32 v45, v153
	v_mov_b32_e32 v46, v153
	v_mov_b32_e32 v47, v153
	v_mov_b32_e32 v52, 0
	v_mov_b32_e32 v53, v153
	v_mov_b32_e32 v54, v153
	v_mov_b32_e32 v55, v153
	v_mov_b32_e32 v8, 0
	v_mov_b32_e32 v9, v153
	v_mov_b32_e32 v10, v153
	v_mov_b32_e32 v11, v153
	v_mov_b32_e32 v16, 0
	v_mov_b32_e32 v17, v153
	v_mov_b32_e32 v18, v153
	v_mov_b32_e32 v19, v153
	v_mov_b32_e32 v24, 0
	v_mov_b32_e32 v25, v153
	v_mov_b32_e32 v26, v153
	v_mov_b32_e32 v27, v153
	v_mov_b32_e32 v32, 0
	v_mov_b32_e32 v33, v153
	v_mov_b32_e32 v34, v153
	v_mov_b32_e32 v35, v153
	v_mov_b32_e32 v40, 0
	v_mov_b32_e32 v41, v153
	v_mov_b32_e32 v42, v153
	v_mov_b32_e32 v43, v153
	v_mov_b32_e32 v48, 0
	v_mov_b32_e32 v49, v153
	v_mov_b32_e32 v50, v153
	v_mov_b32_e32 v51, v153
	v_mov_b32_e32 v56, 0
	v_mov_b32_e32 v57, v153
	v_mov_b32_e32 v58, v153
	v_mov_b32_e32 v59, v153
	v_mov_b32_e32 v60, 0
	v_mov_b32_e32 v61, v153
	v_mov_b32_e32 v62, v153
	v_mov_b32_e32 v63, v153
	v_mov_b32_e32 v64, 0
	v_mov_b32_e32 v65, v153
	v_mov_b32_e32 v66, v153
	v_mov_b32_e32 v67, v153
	v_mov_b32_e32 v68, 0
	v_mov_b32_e32 v69, v153
	v_mov_b32_e32 v70, v153
	v_mov_b32_e32 v71, v153
	v_mov_b32_e32 v76, 0
	v_mov_b32_e32 v77, v153
	v_mov_b32_e32 v78, v153
	v_mov_b32_e32 v79, v153
	v_mov_b32_e32 v84, 0
	v_mov_b32_e32 v85, v153
	v_mov_b32_e32 v86, v153
	v_mov_b32_e32 v87, v153
	v_mov_b32_e32 v92, 0
	v_mov_b32_e32 v93, v153
	v_mov_b32_e32 v94, v153
	v_mov_b32_e32 v95, v153
	v_mov_b32_e32 v100, 0
	v_mov_b32_e32 v101, v153
	v_mov_b32_e32 v102, v153
	v_mov_b32_e32 v103, v153
	v_mov_b32_e32 v104, 0
	v_mov_b32_e32 v105, v153
	v_mov_b32_e32 v106, v153
	v_mov_b32_e32 v107, v153
	v_mov_b32_e32 v108, 0
	v_mov_b32_e32 v109, v153
	v_mov_b32_e32 v110, v153
	v_mov_b32_e32 v111, v153
	v_mov_b32_e32 v72, 0
	v_mov_b32_e32 v73, v153
	v_mov_b32_e32 v74, v153
	v_mov_b32_e32 v75, v153
	v_mov_b32_e32 v80, 0
	v_mov_b32_e32 v81, v153
	v_mov_b32_e32 v82, v153
	v_mov_b32_e32 v83, v153
	v_mov_b32_e32 v88, 0
	v_mov_b32_e32 v89, v153
	v_mov_b32_e32 v90, v153
	v_mov_b32_e32 v91, v153
	v_mov_b32_e32 v96, 0
	v_mov_b32_e32 v97, v153
	v_mov_b32_e32 v98, v153
	v_mov_b32_e32 v99, v153
	v_mov_b32_e32 v112, 0
	v_mov_b32_e32 v113, v153
	v_mov_b32_e32 v114, v153
	v_mov_b32_e32 v115, v153
	v_mov_b32_e32 v116, 0
	v_mov_b32_e32 v117, v153
	v_mov_b32_e32 v118, v153
	v_mov_b32_e32 v119, v153
	v_mov_b32_e32 v120, 0
	v_mov_b32_e32 v121, v153
	v_mov_b32_e32 v122, v153
	v_mov_b32_e32 v123, v153
	v_mov_b32_e32 v124, 0
	v_mov_b32_e32 v125, v153
	v_mov_b32_e32 v126, v153
	v_mov_b32_e32 v127, v153
	s_branch .LBB0_2569
	.p2align	6
.LBB0_2568:
	s_cmpk_lg_i32 s80, 0x180
	s_cbranch_scc1 .Lp11_fast
	v_add_u32_e32 v129, s36, v128
	v_ashrrev_i32_e32 v131, 3, v129
	v_lshlrev_b32_e32 v130, 4, v128
	v_lshlrev_b32_e32 v132, 1, v131
	v_lshrrev_b32_e32 v133, 2, v131
	v_bitop3_b32 v130, v129, s37, v130 bitop3:0x48
	v_and_b32_e32 v132, 24, v132
	v_and_b32_e32 v133, 4, v133
	v_and_b32_e32 v134, 0x1fffe3, v131
	v_lshl_add_u32 v129, v129, 4, v147
	v_or3_b32 v132, v134, v133, v132
	v_ashrrev_i32_e32 v129, 7, v129
	v_lshl_or_b32 v144, v132, 11, v130
	v_lshlrev_b32_e32 v132, 1, v129
	v_lshrrev_b32_e32 v133, 2, v129
	v_and_b32_e32 v132, 24, v132
	v_and_b32_e32 v133, 4, v133
	v_and_b32_e32 v134, 0x1fffe3, v129
	v_or3_b32 v132, v134, v133, v132
	v_lshrrev_b32_e32 v133, 3, v128
	v_lshl_or_b32 v145, v132, 11, v130
	v_and_b32_e32 v132, 15, v128
	v_and_b32_e32 v134, 0xffffffe, v133
	v_bfe_u32 v128, v128, 1, 3
	v_lshlrev_b32_e32 v132, 7, v132
	v_bitop3_b32 v133, v133, v128, s64 bitop3:0x6c
	v_bitop3_b32 v128, v134, v128, 1 bitop3:0x36
	v_or_b32_e32 v146, s58, v132
	v_or_b32_e32 v132, s59, v132
	v_lshlrev_b32_e32 v148, 4, v133
	v_lshlrev_b32_e32 v151, 4, v128
	v_add_u32_e32 v150, v148, v132
	v_add_u32_e32 v152, v151, v132
	v_add_u32_e32 v132, s65, v150
	v_add_u32_e32 v140, s65, v152
	v_add_u32_e32 v158, s66, v150
	v_add_u32_e32 v166, s66, v152
	v_lshl_or_b32 v250, v131, 11, v130
	v_lshl_or_b32 v251, v129, 11, v130
	v_add_u32_e32 v252, 0x40000, v250
	v_add_u32_e32 v253, 0x40000, v251
	v_add3_u32 v148, v148, v146, 0
	v_add3_u32 v146, v151, v146, 0
	s_branch .Lp11_join
	.p2align	6
